# prologue rebalanced after the adaLN speed-up: the 64 workgroups without an adaLN block take 1024 instead of 2048 extra expert weight copy items
# baseline (speedup 1.0000x reference)
;     ...
;     for (int it = it0 + gw; it < it1; it += NGW) {
;         const int e = it / 384, r = it % 384; const size_t eo = (size_t)(layer * 64 + e) * 1024 * 256;
;         if (r < 128) p0_transpose_item(inp(F, I_WGATE) + eo, 1024, 256, UP + (size_t)e * 512 * 1024, 3, scr, r, F.lane);
;         else if (r < 256) p0_transpose_item(inp(F, I_WUP) + eo, 1024, 256, UP + (size_t)e * 512 * 1024, 4, scr, r - 128, F.lane);
;         else p0_transpose_item(inp(F, I_WDOWN) + eo, 256, 1024, DN + (size_t)e * 1024 * 256, 5, scr, r - 256, F.lane, 16.f);
;     }
; __device__ __forceinline__ void p0_prologue(Frame& F) {
;     ...
;         if (P0_BAL > 0 && F.G == 256 && blockIdx.x >= 192) convert_experts(F, 0, CVT0_LATE, CVT0_LATE + P0_BAL, 192, 64);
.LBB0_24:
	s_or_b64 exec, exec, s[0:1]
	s_cmpk_eq_i32 s67, 0x100
	s_cselect_b64 s[0:1], -1, 0
	s_cmpk_gt_u32 s8, 0xbf
	s_cselect_b64 s[2:3], -1, 0
	s_ashr_i32 s14, s9, 6
	s_and_b64 s[0:1], s[0:1], s[2:3]
	s_cmpk_lg_i32 s67, 0x100
	s_cselect_b64 s[40:41], -1, 0
	s_and_b64 s[2:3], s[40:41], exec
	v_and_b32_e32 v35, 63, v6
	s_cselect_b32 s9, s71, s8
	s_and_b64 vcc, exec, s[0:1]
	s_waitcnt lgkmcnt(0)
	s_barrier
	s_cbranch_vccz .LBB0_37
	s_lshl_b32 s0, s8, 3
	s_add_i32 s0, s0, s14
	s_add_i32 s15, s0, 0x1a00
	s_cmpk_gt_i32 s15, 0x23ff
	s_cbranch_scc1 .LBB0_36
	s_add_u32 s1, s38, 0x4800000
	s_addc_u32 s9, s39, 0
	s_add_u32 s16, s38, 0x2800000
	v_lshlrev_b32_e32 v2, 2, v35
	s_addc_u32 s17, s39, 0
	v_and_b32_e32 v1, 56, v6
	v_and_b32_e32 v7, 28, v2
	s_lshl_b32 s18, s15, 6
	s_lshl_b32 s19, s15, 5
	s_lshl_b32 s20, s15, 3
	s_lshl_b32 s21, s15, 1
	s_add_i32 s42, 0, 0x202a8
	v_mov_b32_e32 v9, 0
	s_movk_i32 s43, 0x1000
	s_movk_i32 s44, 0x2000
	s_movk_i32 s45, 0x4000
	s_movk_i32 s46, 0x6000
	s_movk_i32 s47, 0x7000
	s_mov_b32 s0, 0x41800000
	s_movk_i32 s48, 0x7fff
	s_mov_b32 s49, 0xffff0000
	s_mov_b64 s[2:3], 0x600
	s_add_i32 s50, 0, 0x202a0
	s_add_i32 s51, 0, 0x20298
	v_mov_b32_e32 v12, 1
	v_mov_b32_e32 v13, 0x400
	v_mov_b32_e32 v14, 0x7c
	s_branch .LBB0_28
.LBB0_27:
	s_add_i32 s4, s15, 0x200
	s_add_i32 s18, s18, 0x8000
	s_addk_i32 s19, 0x4000
	s_addk_i32 s20, 0x1000
	s_addk_i32 s21, 0x400
	s_cmpk_lt_i32 s15, 0x2200
	s_mov_b32 s15, s4
	global_store_dwordx4 v[10:11], v[2:5], off nt
	s_cbranch_scc0 .LBB0_36

; #define LAS __attribute__((address_space(3)))
; template <class T> __device__ __forceinline__ T* wsp(const Frame& F, size_t off) { return (T*)(F.ws + off); }
;     LAS float* scr = (LAS float*)(F.lds + RING_OFF + F.wave * 16384);
;     const int gw = (ncu ? (int)blockIdx.x - cu0 : F.vcu) * NWAVES + F.wave, NGW = (ncu ? ncu : F.G) * NWAVES;
;     bf16* UP = wsp<bf16>(F, WS_WEUP); bf16* DN = wsp<bf16>(F, WS_WEDN);
;     for (int it = it0 + gw; it < it1; it += NGW) {
;         const int e = it / 384, r = it % 384; const size_t eo = (size_t)(layer * 64 + e) * 1024 * 256;
; __device__ __forceinline__ void p0_prologue(Frame& F) {
;     ...
;     if (P0_PARTS & 4) convert_experts(F, 0, (F.G == 256) ? CVT0_LATE + P0_BAL : 0);
.LBB0_121:
	s_and_b64 s[0:1], s[40:41], exec
	s_cselect_b32 s0, 0, 0x2400
	s_add_i32 s1, s77, s0
	s_cmpk_gt_i32 s1, 0x5fff
	s_cbranch_scc1 .LBB0_132
	s_add_u32 s14, s38, 0x4800000
	s_addc_u32 s15, s39, 0
	s_add_u32 s16, s38, 0x2800000
	v_readlane_b32 s92, v255, 4
	v_readlane_b32 s6, v255, 2
	v_readlane_b32 s28, v255, 0
	s_addc_u32 s17, s39, 0
	v_and_b32_e32 v1, 28, v45
	s_lshl_b32 s18, s1, 6
	s_lshl_b32 s19, s9, 6
	s_lshl_b32 s20, s1, 5
	s_lshl_b32 s21, s9, 5
	s_lshl_b32 s40, s1, 3
	s_lshl_b32 s41, s9, 3
	s_lshl_b32 s42, s1, 1
	s_lshl_b32 s43, s9, 1
	s_add_i32 s44, 0, 0x202a8
	v_mov_b32_e32 v7, 0
	s_movk_i32 s45, 0x1000
	s_movk_i32 s46, 0x2000
	s_movk_i32 s47, 0x4000
	s_movk_i32 s48, 0x6000
	s_movk_i32 s49, 0x7000
	s_mov_b32 s0, 0x41800000
	s_movk_i32 s50, 0x7fff
	s_mov_b32 s51, 0xffff0000
	s_mov_b64 s[2:3], 0x600
	s_add_i32 s52, 0, 0x202a0
	s_add_i32 s53, 0, 0x20298
	v_mov_b32_e32 v10, 1
	v_mov_b32_e32 v11, 0x400
	v_mov_b32_e32 v12, 0x7c
	v_readlane_b32 s93, v255, 5
	v_readlane_b32 s7, v255, 3
	v_readlane_b32 s29, v255, 1
	s_branch .LBB0_124
